# speedup vs baseline: 1.0215x; 1.0215x over previous
_Z4k_l1PKDF16_PKfPKiS4_S4_S4_S4_S4_S4_S2_S2_S0_S0_S2_S2_S2_PDF16_Pf:
	s_load_dwordx2 s[10:11], s[0:1], 0x80
	s_load_dwordx2 s[36:37], s[0:1], 0x68
	s_load_dwordx4 s[16:19], s[0:1], 0x0
	s_load_dwordx4 s[28:31], s[0:1], 0x18
	v_and_b32_e32 v1, 63, v0
	v_lshrrev_b32_e32 v66, 6, v0
	s_cmpk_lt_u32 s2, 27
	s_cbranch_scc0 .Lmy_l1_noprio
	s_setprio 3
	s_branch .Lmy_l1_priodone
.Lmy_l1_noprio:
	v_readfirstlane_b32 s3, v0
	s_lshr_b32 s3, s3, 6
	s_cmp_ge_u32 s3, 4
	s_cbranch_scc0 .Lmy_l1_priodone
	s_setprio 1
